# baseline (speedup 1.0000x reference)
.LBB1_8:
	s_or_b64 exec, exec, s[4:5]
	s_nop 0
	s_waitcnt vmcnt(1)
	v_mov_b32_e32 v184, 1
	v_lshl_add_u32 v180, v176, 2, v172
	v_lshl_add_u32 v181, v177, 2, v172
	v_lshl_add_u32 v182, v178, 2, v172
	v_lshl_add_u32 v183, v179, 2, v172
	s_waitcnt lgkmcnt(0)
	ds_add_u32 v180, v184
	ds_add_u32 v181, v184
	ds_add_u32 v182, v184
	ds_add_u32 v183, v184
	s_waitcnt lgkmcnt(0)
	ds_read_b32 v151, v173
	s_waitcnt lgkmcnt(0)
	v_cvt_f32_i32_e32 v185, v151
	ds_write_b32 v173, v185 offset:256
	v_add_u32_e32 v10, v172, v2
	s_waitcnt vmcnt(1) lgkmcnt(0)
	s_barrier
	ds_read_b128 v[18:21], v10 offset:256
	ds_read_b128 v[22:25], v10 offset:288
	ds_read_b128 v[82:85], v10 offset:320
	ds_read_b128 v[86:89], v10 offset:352
	ds_read_b128 v[74:77], v10 offset:384
	ds_read_b128 v[78:81], v10 offset:416
	ds_read_b128 v[2:5], v213 offset:32768
	ds_read_b128 v[6:9], v213 offset:0
	ds_read_b128 v[66:69], v10 offset:448
	ds_read_b128 v[70:73], v10 offset:480
	ds_read_b128 v[10:13], v213 offset:1024
	s_waitcnt lgkmcnt(3)
	v_pk_mul_f32 v[26:27], v[8:9], v[20:21]
	v_pk_mul_f32 v[28:29], v[6:7], v[18:19]
	ds_read_b128 v[14:17], v213 offset:8192
	s_waitcnt lgkmcnt(1)
	v_pk_mul_f32 v[12:13], v[12:13], v[24:25]
	v_pk_mul_f32 v[10:11], v[10:11], v[22:23]
	v_pk_fma_f32 v[30:31], v[8:9], v[20:21], v[12:13]
	v_pk_fma_f32 v[32:33], v[6:7], v[18:19], v[10:11]
	v_cvt_pk_bf16_f32 v9, v12, v13
	v_cvt_pk_bf16_f32 v7, v26, v27
	v_cvt_pk_bf16_f32 v8, v10, v11
	v_cvt_pk_bf16_f32 v6, v28, v29
	ds_read_b128 v[10:13], v213 offset:33792
	s_nop 0
	v_mfma_f32_32x32x16_bf16 v[34:49], v[2:5], v[6:9], 0
	ds_read_b128 v[6:9], v213 offset:9216
	s_waitcnt lgkmcnt(2)
	v_mul_f32_e32 v26, v16, v20
	v_mul_f32_e32 v27, v17, v21
	v_pk_mul_f32 v[50:51], v[14:15], v[18:19]
	s_mov_b32 s4, 0x3727c5ac
	s_waitcnt lgkmcnt(0)
	v_pk_mul_f32 v[8:9], v[8:9], v[24:25]
	v_pk_mul_f32 v[28:29], v[6:7], v[22:23]
	v_pk_fma_f32 v[90:91], v[16:17], v[20:21], v[8:9]
	v_pk_fma_f32 v[92:93], v[14:15], v[18:19], v[28:29]
	ds_read_b128 v[14:17], v213 offset:2048
	v_cvt_pk_bf16_f32 v9, v8, v9
	v_cvt_pk_bf16_f32 v7, v26, v27
	v_cvt_pk_bf16_f32 v8, v28, v29
	ds_read_b128 v[26:29], v213 offset:3072
	v_cvt_pk_bf16_f32 v6, v50, v51
	s_waitcnt lgkmcnt(1)
	v_pk_mul_f32 v[94:95], v[14:15], v[82:83]
	s_mov_b32 s0, 0x3c800000
	v_mfma_f32_32x32x16_bf16 v[50:65], v[2:5], v[6:9], 0
	v_mul_f32_e32 v2, v16, v84
	v_mul_f32_e32 v3, v17, v85
	s_waitcnt lgkmcnt(0)
	v_mul_f32_e32 v4, v28, v88
	v_mul_f32_e32 v5, v29, v89
	v_pk_mul_f32 v[6:7], v[26:27], v[86:87]
	v_pk_fma_f32 v[8:9], v[16:17], v[84:85], v[4:5]
	v_cvt_pk_bf16_f32 v3, v2, v3
	v_pk_fma_f32 v[14:15], v[14:15], v[82:83], v[6:7]
	v_pk_add_f32 v[26:27], v[8:9], v[30:31]
	v_cvt_pk_bf16_f32 v5, v4, v5
	v_cvt_pk_bf16_f32 v4, v6, v7
	ds_read_b128 v[6:9], v213 offset:10240
	v_pk_add_f32 v[28:29], v[14:15], v[32:33]
	ds_read_b128 v[14:17], v213 offset:11264
	v_cvt_pk_bf16_f32 v2, v94, v95
	s_waitcnt lgkmcnt(1)
	v_pk_mul_f32 v[30:31], v[6:7], v[82:83]
	v_mov_b64_e32 v[152:153], s[4:5]
	v_mfma_f32_32x32x16_bf16 v[34:49], v[10:13], v[2:5], v[34:49]
	v_mul_f32_e32 v2, v8, v84
	v_mul_f32_e32 v3, v9, v85
	s_waitcnt lgkmcnt(0)
	v_mul_f32_e32 v4, v16, v88
	v_mul_f32_e32 v5, v17, v89
	v_pk_mul_f32 v[14:15], v[14:15], v[86:87]
	v_pk_fma_f32 v[8:9], v[8:9], v[84:85], v[4:5]
	v_pk_fma_f32 v[6:7], v[6:7], v[82:83], v[14:15]
	v_cvt_pk_bf16_f32 v5, v4, v5
	v_cvt_pk_bf16_f32 v3, v2, v3
	v_cvt_pk_bf16_f32 v4, v14, v15
	v_pk_add_f32 v[32:33], v[8:9], v[90:91]
	v_pk_add_f32 v[90:91], v[6:7], v[92:93]
	ds_read_b128 v[6:9], v213 offset:34816
	ds_read_b128 v[14:17], v213 offset:4096
	v_cvt_pk_bf16_f32 v2, v30, v31
	s_mov_b32 s13, 0
	s_mov_b64 s[6:7], 0
	v_mfma_f32_32x32x16_bf16 v[50:65], v[10:13], v[2:5], v[50:65]
	ds_read_b128 v[2:5], v213 offset:5120
	ds_read_b128 v[10:13], v213 offset:12288
	s_waitcnt lgkmcnt(2)
	v_pk_mul_f32 v[30:31], v[16:17], v[76:77]
	v_pk_mul_f32 v[92:93], v[14:15], v[74:75]
	s_waitcnt lgkmcnt(1)
	v_pk_mul_f32 v[4:5], v[4:5], v[80:81]
	v_pk_mul_f32 v[94:95], v[2:3], v[78:79]
	v_pk_fma_f32 v[2:3], v[16:17], v[76:77], v[4:5]
	v_cvt_pk_bf16_f32 v5, v4, v5
	v_pk_add_f32 v[96:97], v[2:3], v[26:27]
	v_cvt_pk_bf16_f32 v3, v30, v31
	v_cvt_pk_bf16_f32 v4, v94, v95
	v_cvt_pk_bf16_f32 v2, v92, v93
	v_pk_fma_f32 v[14:15], v[14:15], v[74:75], v[94:95]
	s_waitcnt lgkmcnt(0)
	v_pk_mul_f32 v[30:31], v[10:11], v[74:75]
	v_mfma_f32_32x32x16_bf16 v[34:49], v[6:9], v[2:5], v[34:49]
	ds_read_b128 v[2:5], v213 offset:13312
	v_add_f32_e32 v98, v14, v28
	v_add_f32_e32 v99, v15, v29
	ds_read_b128 v[14:17], v213 offset:35840
	v_pk_mul_f32 v[26:27], v[12:13], v[76:77]
	s_waitcnt lgkmcnt(1)
	v_pk_mul_f32 v[4:5], v[4:5], v[80:81]
	v_pk_mul_f32 v[28:29], v[2:3], v[78:79]
	v_pk_fma_f32 v[2:3], v[12:13], v[76:77], v[4:5]
	v_pk_fma_f32 v[10:11], v[10:11], v[74:75], v[28:29]
	v_pk_add_f32 v[32:33], v[2:3], v[32:33]
	v_pk_add_f32 v[92:93], v[10:11], v[90:91]
	ds_read_b128 v[10:13], v213 offset:6144
	v_cvt_pk_bf16_f32 v5, v4, v5
	v_cvt_pk_bf16_f32 v3, v26, v27
	v_cvt_pk_bf16_f32 v4, v28, v29
	ds_read_b128 v[26:29], v213 offset:7168
	v_cvt_pk_bf16_f32 v2, v30, v31
	s_waitcnt lgkmcnt(1)
	v_pk_mul_f32 v[30:31], v[10:11], v[66:67]
	v_mfma_f32_32x32x16_bf16 v[50:65], v[6:9], v[2:5], v[50:65]
	v_mul_f32_e32 v2, v12, v68
	v_mul_f32_e32 v3, v13, v69
	s_waitcnt lgkmcnt(0)
	v_mul_f32_e32 v4, v28, v72
	v_mul_f32_e32 v5, v29, v73
	v_pk_mul_f32 v[6:7], v[26:27], v[70:71]
	v_pk_fma_f32 v[8:9], v[12:13], v[68:69], v[4:5]
	v_cvt_pk_bf16_f32 v3, v2, v3
	v_pk_fma_f32 v[10:11], v[10:11], v[66:67], v[6:7]
	v_pk_add_f32 v[94:95], v[8:9], v[96:97]
	v_cvt_pk_bf16_f32 v5, v4, v5
	v_cvt_pk_bf16_f32 v4, v6, v7
	ds_read_b128 v[6:9], v213 offset:14336
	v_pk_add_f32 v[96:97], v[10:11], v[98:99]
	ds_read_b128 v[10:13], v213 offset:15360
	v_cvt_pk_bf16_f32 v2, v30, v31
	s_waitcnt lgkmcnt(1)
	v_pk_mul_f32 v[30:31], v[6:7], v[66:67]
	v_mfma_f32_32x32x16_bf16 v[34:49], v[14:17], v[2:5], v[34:49]
	s_waitcnt lgkmcnt(0)
	v_mul_f32_e32 v10, v10, v70
	v_mul_f32_e32 v11, v11, v71
	v_mul_f32_e32 v2, v8, v68
	v_mul_f32_e32 v3, v9, v69
	v_pk_mul_f32 v[4:5], v[12:13], v[72:73]
	v_pk_fma_f32 v[6:7], v[6:7], v[66:67], v[10:11]
	v_pk_fma_f32 v[8:9], v[8:9], v[68:69], v[4:5]
	v_pk_add_f32 v[92:93], v[6:7], v[92:93]
	v_cvt_pk_bf16_f32 v3, v2, v3
	v_pk_add_f32 v[90:91], v[8:9], v[32:33]
	v_cvt_pk_bf16_f32 v5, v4, v5
	v_cvt_pk_bf16_f32 v4, v10, v11
	ds_read_b128 v[26:29], v213 offset:36864
	ds_read_b128 v[6:9], v213 offset:16384
	v_cvt_pk_bf16_f32 v2, v30, v31
	ds_read_b128 v[98:101], v213 offset:25600
	ds_read_b128 v[102:105], v213 offset:37888
	v_mfma_f32_32x32x16_bf16 v[50:65], v[14:17], v[2:5], v[50:65]
	ds_read_b128 v[2:5], v213 offset:17408
	ds_read_b128 v[30:33], v213 offset:24576
	s_waitcnt lgkmcnt(4)
	v_pk_mul_f32 v[12:13], v[6:7], v[18:19]
	v_pk_mul_f32 v[10:11], v[8:9], v[20:21]
	s_waitcnt lgkmcnt(1)
	v_pk_mul_f32 v[14:15], v[2:3], v[22:23]
	v_pk_mul_f32 v[22:23], v[98:99], v[22:23]
	v_pk_fma_f32 v[112:113], v[6:7], v[18:19], v[14:15]
	s_waitcnt lgkmcnt(0)
	v_pk_mul_f32 v[114:115], v[30:31], v[18:19]
	v_pk_fma_f32 v[118:119], v[30:31], v[18:19], v[22:23]
	v_pk_mul_f32 v[4:5], v[4:5], v[24:25]
	v_pk_mul_f32 v[106:107], v[32:33], v[20:21]
	v_pk_mul_f32 v[24:25], v[100:101], v[24:25]
	ds_read_b128 v[98:101], v213 offset:18432
	v_cvt_pk_bf16_f32 v19, v106, v107
	ds_read_b128 v[106:109], v213 offset:19456
	v_pk_fma_f32 v[110:111], v[8:9], v[20:21], v[4:5]
	v_cvt_pk_bf16_f32 v5, v4, v5
	v_cvt_pk_bf16_f32 v3, v10, v11
	v_cvt_pk_bf16_f32 v4, v14, v15
	s_waitcnt lgkmcnt(0)
	v_pk_mul_f32 v[106:107], v[106:107], v[86:87]
	v_cvt_pk_bf16_f32 v2, v12, v13
	v_pk_mul_f32 v[120:121], v[98:99], v[82:83]
	v_pk_mul_f32 v[108:109], v[108:109], v[88:89]
	v_pk_fma_f32 v[98:99], v[98:99], v[82:83], v[106:107]
	v_mfma_f32_32x32x16_bf16 v[2:17], v[26:29], v[2:5], 0
	v_cvt_pk_bf16_f32 v18, v114, v115
	v_mul_f32_e32 v114, v100, v84
	v_mul_f32_e32 v115, v101, v85
	v_fma_f32 v100, v100, v84, v108
	v_fma_f32 v101, v101, v85, v109
	v_pk_add_f32 v[124:125], v[98:99], v[112:113]
	v_pk_add_f32 v[122:123], v[100:101], v[110:111]
	v_cvt_pk_bf16_f32 v101, v108, v109
	v_cvt_pk_bf16_f32 v100, v106, v107
	ds_read_b128 v[106:109], v213 offset:26624
	v_pk_fma_f32 v[116:117], v[32:33], v[20:21], v[24:25]
	v_cvt_pk_bf16_f32 v21, v24, v25
	v_cvt_pk_bf16_f32 v20, v22, v23
	ds_read_b128 v[110:113], v213 offset:27648
	v_cvt_pk_bf16_f32 v99, v114, v115
	v_mfma_f32_32x32x16_bf16 v[18:33], v[26:29], v[18:21], 0
	v_cvt_pk_bf16_f32 v98, v120, v121
	s_waitcnt lgkmcnt(1)
	v_mul_f32_e32 v114, v106, v82
	v_mul_f32_e32 v115, v107, v83
	s_waitcnt lgkmcnt(0)
	v_pk_mul_f32 v[86:87], v[110:111], v[86:87]
	v_pk_mul_f32 v[88:89], v[112:113], v[88:89]
	v_pk_fma_f32 v[82:83], v[106:107], v[82:83], v[86:87]
	v_mfma_f32_32x32x16_bf16 v[2:17], v[102:105], v[98:101], v[2:17]
	v_mul_f32_e32 v98, v108, v84
	v_mul_f32_e32 v99, v109, v85
	v_fma_f32 v84, v108, v84, v88
	v_fma_f32 v85, v109, v85, v89
	v_add_f32_e32 v108, v82, v118
	v_add_f32_e32 v109, v83, v119
	v_cvt_pk_bf16_f32 v83, v98, v99
	v_pk_add_f32 v[106:107], v[84:85], v[116:117]
	v_cvt_pk_bf16_f32 v85, v88, v89
	v_cvt_pk_bf16_f32 v84, v86, v87
	ds_read_b128 v[86:89], v213 offset:38912
	ds_read_b128 v[98:101], v213 offset:20480
	v_cvt_pk_bf16_f32 v82, v114, v115
	s_waitcnt lgkmcnt(0)
	v_pk_mul_f32 v[110:111], v[100:101], v[76:77]
	v_mfma_f32_32x32x16_bf16 v[18:33], v[102:105], v[82:85], v[18:33]
	ds_read_b128 v[82:85], v213 offset:21504
	ds_read_b128 v[102:105], v213 offset:28672
	v_mul_f32_e32 v112, v98, v74
	v_mul_f32_e32 v113, v99, v75
	s_waitcnt lgkmcnt(1)
	v_pk_mul_f32 v[84:85], v[84:85], v[80:81]
	v_pk_mul_f32 v[114:115], v[82:83], v[78:79]
	v_pk_fma_f32 v[82:83], v[100:101], v[76:77], v[84:85]
	v_cvt_pk_bf16_f32 v85, v84, v85
	v_pk_add_f32 v[116:117], v[82:83], v[122:123]
	v_cvt_pk_bf16_f32 v83, v110, v111
	v_cvt_pk_bf16_f32 v84, v114, v115
	v_cvt_pk_bf16_f32 v82, v112, v113
	v_pk_fma_f32 v[98:99], v[98:99], v[74:75], v[114:115]
	s_waitcnt lgkmcnt(0)
	v_pk_mul_f32 v[112:113], v[102:103], v[74:75]
	v_mfma_f32_32x32x16_bf16 v[2:17], v[86:89], v[82:85], v[2:17]
	ds_read_b128 v[82:85], v213 offset:29696
	v_add_f32_e32 v118, v98, v124
	v_add_f32_e32 v119, v99, v125
	v_mul_f32_e32 v110, v104, v76
	v_mul_f32_e32 v111, v105, v77
	ds_read_b128 v[98:101], v213 offset:39936
	s_waitcnt lgkmcnt(1)
	v_pk_mul_f32 v[78:79], v[82:83], v[78:79]
	v_pk_mul_f32 v[80:81], v[84:85], v[80:81]
	v_pk_fma_f32 v[74:75], v[102:103], v[74:75], v[78:79]
	v_pk_fma_f32 v[76:77], v[104:105], v[76:77], v[80:81]
	v_pk_add_f32 v[104:105], v[74:75], v[108:109]
	v_pk_add_f32 v[102:103], v[76:77], v[106:107]
	v_cvt_pk_bf16_f32 v77, v80, v81
	v_cvt_pk_bf16_f32 v76, v78, v79
	ds_read_b128 v[78:81], v213 offset:22528
	ds_read_b128 v[82:85], v213 offset:23552
	v_cvt_pk_bf16_f32 v75, v110, v111
	v_cvt_pk_bf16_f32 v74, v112, v113
	s_waitcnt lgkmcnt(0)
	v_pk_mul_f32 v[82:83], v[82:83], v[70:71]
	v_mfma_f32_32x32x16_bf16 v[18:33], v[86:89], v[74:77], v[18:33]
	v_mul_f32_e32 v74, v80, v68
	v_mul_f32_e32 v75, v81, v69
	v_mul_f32_e32 v76, v84, v72
	v_mul_f32_e32 v77, v85, v73
	v_mul_f32_e32 v86, v78, v66
	v_mul_f32_e32 v87, v79, v67
	v_pk_fma_f32 v[80:81], v[80:81], v[68:69], v[76:77]
	v_pk_fma_f32 v[78:79], v[78:79], v[66:67], v[82:83]
	v_cvt_pk_bf16_f32 v75, v74, v75
	v_pk_add_f32 v[88:89], v[80:81], v[116:117]
	v_pk_add_f32 v[106:107], v[78:79], v[118:119]
	ds_read_b128 v[78:81], v213 offset:30720
	v_cvt_pk_bf16_f32 v77, v76, v77
	v_cvt_pk_bf16_f32 v76, v82, v83
	ds_read_b128 v[82:85], v213 offset:31744
	v_cvt_pk_bf16_f32 v74, v86, v87
	s_waitcnt lgkmcnt(0)
	v_pk_mul_f32 v[72:73], v[84:85], v[72:73]
	v_mfma_f32_32x32x16_bf16 v[2:17], v[98:101], v[74:77], v[2:17]
	v_mul_f32_e32 v74, v80, v68
	v_mul_f32_e32 v75, v81, v69
	v_fma_f32 v68, v80, v68, v72
	v_fma_f32 v69, v81, v69, v73
	v_mul_f32_e32 v70, v82, v70
	v_mul_f32_e32 v71, v83, v71
	v_pk_add_f32 v[84:85], v[68:69], v[102:103]
	v_cvt_pk_bf16_f32 v69, v72, v73
	v_pk_mov_b32 v[72:73], v[96:97], v[94:95] op_sel:[1,0]
	v_mov_b32_e32 v97, v95
	v_pk_add_f32 v[72:73], v[72:73], v[96:97]
	v_pk_mul_f32 v[76:77], v[78:79], v[66:67]
	v_pk_fma_f32 v[66:67], v[78:79], v[66:67], v[70:71]
	v_pk_add_f32 v[72:73], v[72:73], v[72:73] op_sel:[0,1] op_sel_hi:[1,0]
	v_pk_add_f32 v[86:87], v[66:67], v[104:105]
	v_mov_b32_e32 v66, v72
	s_nop 1
	v_permlane32_swap_b32_e32 v72, v66
	v_add_f32_e32 v66, v72, v66
	v_cvt_pk_bf16_f32 v67, v74, v75
	v_rcp_f32_e32 v74, v66
	v_cvt_pk_bf16_f32 v68, v70, v71
	v_cvt_pk_bf16_f32 v66, v76, v77
	v_pk_mul_f32 v[70:71], v[46:47], v[74:75] op_sel_hi:[1,0]
	s_nop 0
	v_mfma_f32_32x32x16_bf16 v[18:33], v[98:101], v[66:69], v[18:33]
	v_mul_f32_e32 v66, v42, v74
	v_mul_f32_e32 v67, v43, v74
	v_pk_mov_b32 v[42:43], v[92:93], v[90:91] op_sel:[1,0]
	v_mov_b32_e32 v93, v91
	v_pk_add_f32 v[42:43], v[42:43], v[92:93]
	v_pk_mul_f32 v[68:69], v[44:45], v[74:75] op_sel_hi:[1,0]
	v_pk_add_f32 v[42:43], v[42:43], v[42:43] op_sel:[0,1] op_sel_hi:[1,0]
	v_pk_mov_b32 v[44:45], v[106:107], v[88:89] op_sel:[1,0]
	v_mov_b32_e32 v43, v42
	s_nop 1
	v_permlane32_swap_b32_e32 v42, v43
	v_add_f32_e32 v42, v42, v43
	v_rcp_f32_e32 v42, v42
	v_mov_b32_e32 v107, v89
	v_pk_add_f32 v[44:45], v[44:45], v[106:107]
	v_pk_mul_f32 v[72:73], v[48:49], v[74:75] op_sel_hi:[1,0]
	v_pk_add_f32 v[44:45], v[44:45], v[44:45] op_sel:[0,1] op_sel_hi:[1,0]
	v_pk_mul_f32 v[36:37], v[36:37], v[74:75] op_sel_hi:[1,0]
	v_pk_mul_f32 v[38:39], v[38:39], v[74:75] op_sel_hi:[1,0]
	v_pk_mul_f32 v[40:41], v[40:41], v[74:75] op_sel_hi:[1,0]
	v_pk_mul_f32 v[34:35], v[34:35], v[74:75] op_sel_hi:[1,0]
	v_pk_mul_f32 v[74:75], v[58:59], v[42:43] op_sel_hi:[1,0]
	v_pk_mul_f32 v[78:79], v[60:61], v[42:43] op_sel_hi:[1,0]
	v_pk_mul_f32 v[80:81], v[62:63], v[42:43] op_sel_hi:[1,0]
	v_pk_mul_f32 v[82:83], v[64:65], v[42:43] op_sel_hi:[1,0]
	v_pk_mul_f32 v[92:93], v[52:53], v[42:43] op_sel_hi:[1,0]
	v_mov_b32_e32 v43, v44
	s_nop 1
	v_permlane32_swap_b32_e32 v44, v43
	v_add_f32_e32 v43, v44, v43
	v_rcp_f32_e32 v76, v43
	v_pk_mul_f32 v[96:97], v[54:55], v[42:43] op_sel_hi:[1,0]
	v_pk_mul_f32 v[94:95], v[56:57], v[42:43] op_sel_hi:[1,0]
	v_pk_mul_f32 v[98:99], v[50:51], v[42:43] op_sel_hi:[1,0]
	v_pk_mul_f32 v[100:101], v[4:5], v[76:77] op_sel_hi:[1,0]
	v_pk_mov_b32 v[4:5], v[86:87], v[84:85] op_sel:[1,0]
	v_mov_b32_e32 v87, v85
	v_pk_add_f32 v[4:5], v[4:5], v[86:87]
	v_pk_mul_f32 v[102:103], v[6:7], v[76:77] op_sel_hi:[1,0]
	v_pk_add_f32 v[104:105], v[4:5], v[4:5] op_sel:[0,1] op_sel_hi:[1,0]
	v_cvt_pk_bf16_f32 v7, v40, v41
	ds_read_b128 v[84:87], v150 offset:52224
	ds_read_b128 v[50:53], v150 offset:35840
	ds_read_b128 v[54:57], v150 offset:36864
	ds_read_b128 v[58:61], v150 offset:37888
	ds_read_b128 v[62:65], v150 offset:38912
	v_cvt_pk_bf16_f32 v6, v38, v39
	v_cvt_pk_bf16_f32 v5, v36, v37
	v_cvt_pk_bf16_f32 v4, v34, v35
	ds_read_b128 v[88:91], v150 offset:53248
	ds_read_b128 v[34:37], v150 offset:39936
	ds_read_b128 v[38:41], v150 offset:40960
	ds_read_b128 v[42:45], v150 offset:41984
	ds_read_b128 v[46:49], v150 offset:43008
	v_cvt_pk_bf16_f32 v95, v94, v95
	v_cvt_pk_bf16_f32 v94, v96, v97
	v_cvt_pk_bf16_f32 v93, v92, v93
	v_cvt_pk_bf16_f32 v92, v98, v99
	s_waitcnt lgkmcnt(5)
	v_mfma_f32_32x32x16_bf16 v[50:65], v[84:87], v[4:7], v[50:65]
	v_mul_f32_e32 v10, v10, v76
	v_mul_f32_e32 v11, v11, v76
	v_mul_f32_e32 v12, v12, v76
	v_mul_f32_e32 v13, v13, v76
	v_mul_f32_e32 v8, v8, v76
	v_mul_f32_e32 v9, v9, v76
	v_mov_b32_e32 v77, v104
	s_nop 1
	v_permlane32_swap_b32_e32 v104, v77
	v_cvt_pk_bf16_f32 v73, v72, v73
	s_waitcnt lgkmcnt(0)
	v_mfma_f32_32x32x16_bf16 v[34:49], v[84:87], v[92:95], v[34:49]
	v_cvt_pk_bf16_f32 v72, v70, v71
	v_cvt_pk_bf16_f32 v70, v66, v67
	v_add_f32_e32 v66, v104, v77
	v_cvt_pk_bf16_f32 v71, v68, v69
	v_rcp_f32_e32 v104, v66
	v_cvt_pk_bf16_f32 v69, v82, v83
	v_cvt_pk_bf16_f32 v68, v80, v81
	v_cvt_pk_bf16_f32 v67, v78, v79
	v_cvt_pk_bf16_f32 v66, v74, v75
	ds_read_b128 v[78:81], v150 offset:54272
	v_mfma_f32_32x32x16_bf16 v[50:65], v[88:91], v[70:73], v[50:65]
	v_mul_f32_e32 v2, v2, v76
	v_mul_f32_e32 v3, v3, v76
	v_mul_f32_e32 v20, v20, v104
	v_mul_f32_e32 v21, v21, v104
	v_cvt_pk_bf16_f32 v85, v8, v9
	v_cvt_pk_bf16_f32 v82, v2, v3
	v_pk_mul_f32 v[2:3], v[22:23], v[104:105] op_sel_hi:[1,0]
	v_pk_mul_f32 v[8:9], v[24:25], v[104:105] op_sel_hi:[1,0]
	v_pk_mul_f32 v[18:19], v[18:19], v[104:105] op_sel_hi:[1,0]
	v_mfma_f32_32x32x16_bf16 v[34:49], v[88:91], v[66:69], v[34:49]
	v_cvt_pk_bf16_f32 v84, v102, v103
	v_cvt_pk_bf16_f32 v83, v100, v101
	ds_read_b128 v[86:89], v150 offset:55296
	v_cvt_pk_bf16_f32 v99, v8, v9
	v_cvt_pk_bf16_f32 v98, v2, v3
	v_cvt_pk_bf16_f32 v97, v20, v21
	v_cvt_pk_bf16_f32 v96, v18, v19
	s_waitcnt lgkmcnt(1)
	v_mfma_f32_32x32x16_bf16 v[50:65], v[78:81], v[82:85], v[50:65]
	v_mul_f32_e32 v2, v14, v76
	v_mul_f32_e32 v3, v15, v76
	v_mul_f32_e32 v8, v16, v76
	v_mul_f32_e32 v9, v17, v76
	v_mul_f32_e32 v14, v26, v104
	v_mul_f32_e32 v15, v27, v104
	v_cvt_pk_bf16_f32 v77, v8, v9
	v_cvt_pk_bf16_f32 v76, v2, v3
	v_cvt_pk_bf16_f32 v74, v10, v11
	v_pk_mul_f32 v[2:3], v[28:29], v[104:105] op_sel_hi:[1,0]
	v_mfma_f32_32x32x16_bf16 v[34:49], v[78:81], v[96:99], v[34:49]
	v_mul_f32_e32 v8, v30, v104
	v_mul_f32_e32 v9, v31, v104
	v_mul_f32_e32 v10, v32, v104
	v_mul_f32_e32 v11, v33, v104
	v_cvt_pk_bf16_f32 v75, v12, v13
	v_cvt_pk_bf16_f32 v81, v10, v11
	v_cvt_pk_bf16_f32 v80, v8, v9
	v_cvt_pk_bf16_f32 v79, v2, v3
	v_cvt_pk_bf16_f32 v78, v14, v15
	s_waitcnt lgkmcnt(0)
	v_mfma_f32_32x32x16_bf16 v[50:65], v[86:89], v[74:77], v[50:65]
	v_mfma_f32_32x32x16_bf16 v[34:49], v[86:89], v[78:81], v[34:49]
	ds_read_b128 v[86:89], v150 offset:56320
	ds_read_b128 v[18:21], v150 offset:44032
	ds_read_b128 v[22:25], v150 offset:45056
	ds_read_b128 v[26:29], v150 offset:46080
	ds_read_b128 v[30:33], v150 offset:47104
	ds_read_b128 v[100:103], v150 offset:57344
	s_waitcnt lgkmcnt(1)
	v_mfma_f32_32x32x16_bf16 v[18:33], v[86:89], v[4:7], v[18:33]
	ds_read_b128 v[2:5], v150 offset:48128
	ds_read_b128 v[6:9], v150 offset:49152
	ds_read_b128 v[10:13], v150 offset:50176
	ds_read_b128 v[14:17], v150 offset:51200
	s_waitcnt lgkmcnt(0)
	v_mfma_f32_32x32x16_bf16 v[2:17], v[86:89], v[92:95], v[2:17]
	v_mfma_f32_32x32x16_bf16 v[18:33], v[100:103], v[70:73], v[18:33]
	v_mfma_f32_32x32x16_bf16 v[2:17], v[100:103], v[66:69], v[2:17]
	ds_read_b128 v[66:69], v150 offset:58368
	ds_read_b128 v[70:73], v150 offset:59392
	s_waitcnt lgkmcnt(1)
	v_mfma_f32_32x32x16_bf16 v[18:33], v[66:69], v[82:85], v[18:33]
	v_mfma_f32_32x32x16_bf16 v[2:17], v[66:69], v[96:99], v[2:17]
	s_waitcnt lgkmcnt(0)
	v_mfma_f32_32x32x16_bf16 v[18:33], v[70:73], v[74:77], v[18:33]
	v_mfma_f32_32x32x16_bf16 v[2:17], v[70:73], v[78:81], v[2:17]
	s_nop 10
	v_mul_f32_e32 v66, v22, v22
	v_mul_f32_e32 v67, v23, v23
	v_mul_f32_e32 v68, v30, v30
	v_mul_f32_e32 v69, v31, v31
	v_mul_f32_e32 v70, v24, v24
	v_mul_f32_e32 v71, v25, v25
	v_pk_mul_f32 v[72:73], v[32:33], v[32:33]
	v_pk_mul_f32 v[74:75], v[20:21], v[20:21]
	v_pk_mul_f32 v[76:77], v[28:29], v[28:29]
	v_pk_mul_f32 v[78:79], v[26:27], v[26:27]
	v_pk_mul_f32 v[80:81], v[18:19], v[18:19]
	v_pk_fma_f32 v[78:79], v[58:59], v[58:59], v[78:79]
	v_pk_fma_f32 v[76:77], v[60:61], v[60:61], v[76:77]
	v_pk_fma_f32 v[74:75], v[52:53], v[52:53], v[74:75]
	v_pk_fma_f32 v[72:73], v[64:65], v[64:65], v[72:73]
	v_pk_fma_f32 v[70:71], v[56:57], v[56:57], v[70:71]
	v_pk_fma_f32 v[68:69], v[62:63], v[62:63], v[68:69]
	v_pk_fma_f32 v[66:67], v[54:55], v[54:55], v[66:67]
	v_pk_fma_f32 v[80:81], v[50:51], v[50:51], v[80:81]
	v_pk_add_f32 v[66:67], v[66:67], v[68:69]
	v_pk_add_f32 v[68:69], v[70:71], v[72:73]
	v_pk_add_f32 v[70:71], v[74:75], v[76:77]
	v_pk_add_f32 v[72:73], v[80:81], v[78:79]
	v_pk_add_f32 v[68:69], v[70:71], v[68:69]
	v_pk_add_f32 v[66:67], v[72:73], v[66:67]
	v_pk_mul_f32 v[72:73], v[14:15], v[14:15]
	v_pk_mov_b32 v[70:71], v[66:67], v[68:69] op_sel:[1,0]
	v_mov_b32_e32 v67, v69
	v_pk_add_f32 v[66:67], v[70:71], v[66:67]
	v_pk_mul_f32 v[70:71], v[6:7], v[6:7]
	v_pk_mul_f32 v[74:75], v[8:9], v[8:9]
	v_pk_mul_f32 v[76:77], v[16:17], v[16:17]
	v_pk_mul_f32 v[78:79], v[4:5], v[4:5]
	v_pk_mul_f32 v[80:81], v[12:13], v[12:13]
	v_pk_mul_f32 v[82:83], v[10:11], v[10:11]
	v_pk_mul_f32 v[84:85], v[2:3], v[2:3]
	v_pk_fma_f32 v[82:83], v[42:43], v[42:43], v[82:83]
	v_pk_fma_f32 v[80:81], v[44:45], v[44:45], v[80:81]
	v_pk_fma_f32 v[78:79], v[36:37], v[36:37], v[78:79]
	v_pk_fma_f32 v[76:77], v[48:49], v[48:49], v[76:77]
	v_pk_fma_f32 v[74:75], v[40:41], v[40:41], v[74:75]
	v_pk_fma_f32 v[72:73], v[46:47], v[46:47], v[72:73]
	v_pk_fma_f32 v[70:71], v[38:39], v[38:39], v[70:71]
	v_pk_fma_f32 v[84:85], v[34:35], v[34:35], v[84:85]
	v_pk_add_f32 v[70:71], v[70:71], v[72:73]
	v_pk_add_f32 v[72:73], v[74:75], v[76:77]
	v_pk_add_f32 v[74:75], v[78:79], v[80:81]
	v_pk_add_f32 v[76:77], v[84:85], v[82:83]
	v_pk_add_f32 v[72:73], v[74:75], v[72:73]
	v_pk_add_f32 v[70:71], v[76:77], v[70:71]
	v_pk_add_f32 v[66:67], v[66:67], v[66:67] op_sel:[0,1] op_sel_hi:[1,0]
	v_pk_mov_b32 v[74:75], v[70:71], v[72:73] op_sel:[1,0]
	v_mov_b32_e32 v71, v73
	v_pk_add_f32 v[70:71], v[74:75], v[70:71]
	v_mov_b32_e32 v69, v66
	v_pk_add_f32 v[70:71], v[70:71], v[70:71] op_sel:[0,1] op_sel_hi:[1,0]
	s_nop 0
	v_permlane32_swap_b32_e32 v66, v69
	v_mov_b32_e32 v68, v70
	s_nop 1
	v_permlane32_swap_b32_e32 v70, v68
	v_mov_b32_e32 v71, v66
	v_pk_add_f32 v[66:67], v[70:71], v[68:69]
	v_pk_fma_f32 v[66:67], v[66:67], s[0:1], v[152:153] op_sel_hi:[1,0,0]
	s_mov_b32 s1, 0x800000
	v_mul_f32_e32 v68, 0x4b800000, v67
	v_cmp_gt_f32_e32 vcc, s1, v67
	s_nop 1
	v_cndmask_b32_e32 v67, v67, v68, vcc
	v_rsq_f32_e32 v67, v67
	s_nop 0
	v_mul_f32_e32 v68, 0x45800000, v67
	v_cndmask_b32_e32 v68, v67, v68, vcc
	v_pk_mul_f32 v[158:159], v[50:51], v[68:69] op_sel_hi:[1,0]
	v_pk_mul_f32 v[50:51], v[18:19], v[68:69] op_sel_hi:[1,0]
	v_mul_f32_e32 v18, 0x4b800000, v66
	v_cmp_gt_f32_e32 vcc, s1, v66
	v_pk_mul_f32 v[80:81], v[60:61], v[68:69] op_sel_hi:[1,0]
	v_pk_mul_f32 v[60:61], v[28:29], v[68:69] op_sel_hi:[1,0]
	v_cndmask_b32_e32 v18, v66, v18, vcc
	v_rsq_f32_e32 v18, v18
	v_pk_mul_f32 v[78:79], v[58:59], v[68:69] op_sel_hi:[1,0]
	v_pk_mul_f32 v[160:161], v[52:53], v[68:69] op_sel_hi:[1,0]
	v_pk_mul_f32 v[82:83], v[54:55], v[68:69] op_sel_hi:[1,0]
	v_mul_f32_e32 v19, 0x45800000, v18
	v_cndmask_b32_e32 v28, v18, v19, vcc
	v_pk_mul_f32 v[168:169], v[56:57], v[68:69] op_sel_hi:[1,0]
	v_pk_mul_f32 v[58:59], v[26:27], v[68:69] op_sel_hi:[1,0]
	v_pk_mul_f32 v[52:53], v[20:21], v[68:69] op_sel_hi:[1,0]
	v_pk_mul_f32 v[54:55], v[22:23], v[68:69] op_sel_hi:[1,0]
	v_pk_mul_f32 v[56:57], v[24:25], v[68:69] op_sel_hi:[1,0]
	v_pk_mul_f32 v[18:19], v[42:43], v[28:29] op_sel_hi:[1,0]
	v_pk_mul_f32 v[20:21], v[44:45], v[28:29] op_sel_hi:[1,0]
	v_pk_mul_f32 v[22:23], v[46:47], v[28:29] op_sel_hi:[1,0]
	v_pk_mul_f32 v[26:27], v[48:49], v[28:29] op_sel_hi:[1,0]
	v_pk_mul_f32 v[162:163], v[34:35], v[28:29] op_sel_hi:[1,0]
	v_pk_mul_f32 v[164:165], v[36:37], v[28:29] op_sel_hi:[1,0]
	v_pk_mul_f32 v[166:167], v[38:39], v[28:29] op_sel_hi:[1,0]
	v_pk_mul_f32 v[24:25], v[40:41], v[28:29] op_sel_hi:[1,0]
	v_pk_mul_f32 v[104:105], v[2:3], v[28:29] op_sel_hi:[1,0]
	v_pk_mul_f32 v[112:113], v[4:5], v[28:29] op_sel_hi:[1,0]
	ds_read_b128 v[2:5], v150 offset:60416
	ds_read_b128 v[34:37], v174 offset:32768
	ds_read_b128 v[38:41], v174 offset:32800
	ds_read_b128 v[42:45], v174 offset:32832
	ds_read_b128 v[46:49], v174 offset:32864
	v_cvt_pk_bf16_f32 v129, v168, v169
	v_cvt_pk_bf16_f32 v128, v82, v83
	v_cvt_pk_bf16_f32 v127, v160, v161
	v_cvt_pk_bf16_f32 v126, v158, v159
	v_cvt_pk_bf16_f32 v137, v24, v25
	v_cvt_pk_bf16_f32 v136, v166, v167
	v_cvt_pk_bf16_f32 v135, v164, v165
	s_waitcnt lgkmcnt(0)
	v_mfma_f32_32x32x16_bf16 v[86:101], v[2:5], v[126:129], v[34:49]
	v_cvt_pk_bf16_f32 v134, v162, v163
	v_mul_f32_e32 v84, v62, v68
	v_mul_f32_e32 v85, v63, v68
	v_mul_f32_e32 v170, v64, v68
	v_mul_f32_e32 v171, v65, v68
	v_pk_mul_f32 v[62:63], v[30:31], v[68:69] op_sel_hi:[1,0]
	v_pk_mul_f32 v[64:65], v[32:33], v[68:69] op_sel_hi:[1,0]
	v_pk_mul_f32 v[116:117], v[6:7], v[28:29] op_sel_hi:[1,0]
	v_pk_mul_f32 v[154:155], v[8:9], v[28:29] op_sel_hi:[1,0]
	v_mfma_f32_32x32x16_bf16 v[34:49], v[2:5], v[134:137], v[34:49]
	ds_read_b128 v[6:9], v150 offset:61440
	ds_read_b128 v[66:69], v174 offset:32896
	ds_read_b128 v[106:109], v150 offset:64512
	v_cvt_pk_bf16_f32 v125, v170, v171
	v_cvt_pk_bf16_f32 v124, v84, v85
	v_cvt_pk_bf16_f32 v123, v80, v81
	v_cvt_pk_bf16_f32 v122, v78, v79
	v_cvt_pk_bf16_f32 v149, v26, v27
	v_cvt_pk_bf16_f32 v148, v22, v23
	v_cvt_pk_bf16_f32 v147, v20, v21
	v_cvt_pk_bf16_f32 v146, v18, v19
	s_waitcnt lgkmcnt(2)
	v_mfma_f32_32x32x16_bf16 v[86:101], v[6:9], v[122:125], v[86:101]
	v_mul_f32_e32 v102, v10, v28
	v_mul_f32_e32 v103, v11, v28
	v_mul_f32_e32 v110, v12, v28
	v_mul_f32_e32 v111, v13, v28
	v_mul_f32_e32 v114, v14, v28
	v_mul_f32_e32 v115, v15, v28
	v_pk_mul_f32 v[156:157], v[16:17], v[28:29] op_sel_hi:[1,0]
	ds_read_b128 v[176:179], v174 offset:33536
	ds_read_b128 v[180:183], v174 offset:33568
	ds_read_b128 v[184:187], v174 offset:33600
	ds_read_b128 v[28:31], v174 offset:33632
	ds_read_b128 v[188:191], v174 offset:33792
	ds_read_b128 v[192:195], v174 offset:33824
	ds_read_b128 v[196:199], v174 offset:33856
	ds_read_b128 v[200:203], v174 offset:33888
	ds_read_b128 v[204:207], v150 offset:62464
	v_cvt_pk_bf16_f32 v133, v56, v57
	v_mfma_f32_32x32x16_bf16 v[34:49], v[6:9], v[146:149], v[34:49]
	v_cvt_pk_bf16_f32 v132, v54, v55
	v_cvt_pk_bf16_f32 v131, v52, v53
	v_cvt_pk_bf16_f32 v130, v50, v51
	ds_read_b128 v[70:73], v174 offset:33664
	ds_read_b128 v[74:77], v174 offset:33920
	ds_read_b128 v[208:211], v150 offset:63488
	v_cvt_pk_bf16_f32 v145, v154, v155
	v_cvt_pk_bf16_f32 v144, v116, v117
	v_cvt_pk_bf16_f32 v143, v112, v113
	v_cvt_pk_bf16_f32 v142, v104, v105
	s_waitcnt lgkmcnt(3)
	v_mfma_f32_32x32x16_bf16 v[86:101], v[204:207], v[130:133], v[86:101]
	v_cvt_pk_bf16_f32 v121, v64, v65
	v_cvt_pk_bf16_f32 v120, v62, v63
	v_cvt_pk_bf16_f32 v119, v60, v61
	v_cvt_pk_bf16_f32 v118, v58, v59
	v_cvt_pk_bf16_f32 v141, v156, v157
	v_cvt_pk_bf16_f32 v140, v114, v115
	v_cvt_pk_bf16_f32 v139, v110, v111
	v_mfma_f32_32x32x16_bf16 v[34:49], v[204:207], v[142:145], v[34:49]
	v_cvt_pk_bf16_f32 v138, v102, v103
	v_fma_f32 v16, v30, v170, v202
	v_fma_f32 v17, v31, v171, v203
	v_fma_f32 v14, v28, v84, v200
	v_fma_f32 v15, v29, v85, v201
	v_pk_fma_f32 v[12:13], v[186:187], v[80:81], v[198:199]
	v_pk_fma_f32 v[10:11], v[184:185], v[78:79], v[196:197]
	v_pk_fma_f32 v[8:9], v[182:183], v[168:169], v[194:195]
	s_waitcnt lgkmcnt(0)
	v_mfma_f32_32x32x16_bf16 v[86:101], v[208:211], v[118:121], v[86:101]
	v_fma_f32 v6, v180, v82, v192
	v_fma_f32 v7, v181, v83, v193
	ds_read_b128 v[78:81], v174 offset:33760
	ds_read_b128 v[82:85], v174 offset:33248
	v_fma_f32 v4, v178, v160, v190
	v_fma_f32 v5, v179, v161, v191
	v_pk_fma_f32 v[2:3], v[176:177], v[158:159], v[188:189]
	v_pk_fma_f32 v[32:33], v[30:31], v[26:27], v[202:203]
	v_pk_fma_f32 v[30:31], v[28:29], v[22:23], v[200:201]
	v_pk_fma_f32 v[28:29], v[186:187], v[20:21], v[198:199]
	v_pk_fma_f32 v[26:27], v[184:185], v[18:19], v[196:197]
	v_pk_fma_f32 v[24:25], v[182:183], v[24:25], v[194:195]
	v_pk_fma_f32 v[22:23], v[180:181], v[166:167], v[192:193]
	v_pk_fma_f32 v[20:21], v[178:179], v[164:165], v[190:191]
	v_pk_fma_f32 v[18:19], v[176:177], v[162:163], v[188:189]
	ds_read_b128 v[158:161], v174 offset:33696
	ds_read_b128 v[162:165], v174 offset:33728
	ds_read_b128 v[166:169], v174 offset:33952
	ds_read_b128 v[176:179], v174 offset:33984
	ds_read_b128 v[180:183], v174 offset:34016
	ds_read_b128 v[184:187], v212 offset:11264
	v_mfma_f32_32x32x16_bf16 v[34:49], v[208:211], v[138:141], v[34:49]
	v_cvt_pk_bf16_f32 v86, v86, v87
	v_cvt_pk_bf16_f32 v87, v88, v89
	v_cvt_pk_bf16_f32 v88, v90, v91
	v_cvt_pk_bf16_f32 v89, v92, v93
	ds_read_b128 v[90:93], v212 offset:12288
	v_pk_max_i16 v86, v86, 0
	v_pk_max_i16 v87, v87, 0
	v_pk_max_i16 v88, v88, 0
	v_pk_max_i16 v89, v89, 0
	s_nop 1
	s_nop 0
	v_cvt_pk_bf16_f32 v188, v34, v35
	v_cvt_pk_bf16_f32 v189, v36, v37
	v_cvt_pk_bf16_f32 v190, v38, v39
	v_cvt_pk_bf16_f32 v191, v40, v41
	s_waitcnt lgkmcnt(1)
	v_mfma_f32_32x32x16_bf16 v[2:17], v[184:187], v[86:89], v[2:17]
	v_pk_max_i16 v188, v188, 0
	v_pk_max_i16 v189, v189, 0
	v_pk_max_i16 v190, v190, 0
	v_pk_max_i16 v191, v191, 0
	v_cvt_pk_bf16_f32 v94, v94, v95
	v_cvt_pk_bf16_f32 v95, v96, v97
	v_cvt_pk_bf16_f32 v96, v98, v99
	v_cvt_pk_bf16_f32 v97, v100, v101
	v_cvt_pk_bf16_f32 v98, v42, v43
	v_cvt_pk_bf16_f32 v99, v44, v45
	v_mfma_f32_32x32x16_bf16 v[18:33], v[184:187], v[188:191], v[18:33]
	ds_read_b128 v[184:187], v212 offset:19456
	v_cvt_pk_bf16_f32 v100, v46, v47
	v_cvt_pk_bf16_f32 v101, v48, v49
	v_fma_f32 v64, v80, v64, v182
	v_fma_f32 v65, v81, v65, v183
	v_pk_fma_f32 v[62:63], v[78:79], v[62:63], v[180:181]
	v_pk_fma_f32 v[60:61], v[164:165], v[60:61], v[178:179]
	v_pk_fma_f32 v[58:59], v[162:163], v[58:59], v[176:177]
	v_pk_max_i16 v94, v94, 0
	v_pk_max_i16 v95, v95, 0
	v_pk_max_i16 v96, v96, 0
	v_pk_max_i16 v97, v97, 0
	v_pk_max_i16 v98, v98, 0
	v_pk_max_i16 v99, v99, 0
	v_pk_max_i16 v100, v100, 0
	v_pk_max_i16 v101, v101, 0
	v_pk_fma_f32 v[56:57], v[160:161], v[56:57], v[168:169]
	s_waitcnt lgkmcnt(1)
	v_mfma_f32_32x32x16_bf16 v[2:17], v[90:93], v[94:97], v[2:17]
	v_fma_f32 v54, v158, v54, v166
	v_fma_f32 v55, v159, v55, v167
	v_fma_f32 v52, v72, v52, v76
	v_fma_f32 v53, v73, v53, v77
	v_fma_f32 v50, v70, v50, v74
	v_fma_f32 v51, v71, v51, v75
	v_pk_fma_f32 v[48:49], v[80:81], v[156:157], v[182:183]
	v_pk_fma_f32 v[46:47], v[78:79], v[114:115], v[180:181]
	v_pk_fma_f32 v[44:45], v[164:165], v[110:111], v[178:179]
	v_pk_fma_f32 v[42:43], v[162:163], v[102:103], v[176:177]
	v_mfma_f32_32x32x16_bf16 v[18:33], v[90:93], v[98:101], v[18:33]
	ds_read_b128 v[90:93], v212 offset:20480
	v_fma_f32 v40, v160, v154, v168
	v_fma_f32 v41, v161, v155, v169
	v_fma_f32 v38, v158, v116, v166
	v_fma_f32 v39, v159, v117, v167
	v_pk_fma_f32 v[36:37], v[72:73], v[112:113], v[76:77]
	v_pk_fma_f32 v[34:35], v[70:71], v[104:105], v[74:75]
	s_waitcnt lgkmcnt(1)
	v_mfma_f32_32x32x16_bf16 v[50:65], v[184:187], v[86:89], v[50:65]
	ds_read_b128 v[70:73], v174 offset:32928
	ds_read_b128 v[74:77], v174 offset:32960
	ds_read_b128 v[78:81], v174 offset:32992
	ds_read_b128 v[86:89], v174 offset:33024
	ds_read_b128 v[110:113], v212 offset:1024
	v_mfma_f32_32x32x16_bf16 v[34:49], v[184:187], v[188:191], v[34:49]
	s_waitcnt lgkmcnt(5)
	v_mfma_f32_32x32x16_bf16 v[50:65], v[90:93], v[94:97], v[50:65]
	v_mfma_f32_32x32x16_bf16 v[34:49], v[90:93], v[98:101], v[34:49]
	s_waitcnt lgkmcnt(2)
	v_mfma_f32_32x32x16_bf16 v[90:105], v[106:109], v[126:129], v[66:81]
	v_mfma_f32_32x32x16_bf16 v[66:81], v[106:109], v[134:137], v[66:81]
	ds_read_b128 v[106:109], v212 offset:0
	s_waitcnt lgkmcnt(0)
	v_mfma_f32_32x32x16_bf16 v[90:105], v[106:109], v[122:125], v[90:105]
	v_mfma_f32_32x32x16_bf16 v[66:81], v[106:109], v[146:149], v[66:81]
	ds_read_b128 v[106:109], v212 offset:2048
	v_mfma_f32_32x32x16_bf16 v[90:105], v[110:113], v[130:133], v[90:105]
	v_mfma_f32_32x32x16_bf16 v[66:81], v[110:113], v[142:145], v[66:81]
	ds_read_b128 v[110:113], v212 offset:13312
	s_waitcnt lgkmcnt(1)
	v_mfma_f32_32x32x16_bf16 v[90:105], v[106:109], v[118:121], v[90:105]
	v_mfma_f32_32x32x16_bf16 v[66:81], v[106:109], v[138:141], v[66:81]
	s_nop 10
	v_cvt_pk_bf16_f32 v90, v90, v91
	v_cvt_pk_bf16_f32 v91, v92, v93
	v_cvt_pk_bf16_f32 v92, v94, v95
	v_cvt_pk_bf16_f32 v94, v98, v99
	v_cvt_pk_bf16_f32 v95, v100, v101
	ds_read_b128 v[98:101], v212 offset:21504
	v_cvt_pk_bf16_f32 v66, v66, v67
	v_cvt_pk_bf16_f32 v67, v68, v69
	v_cvt_pk_bf16_f32 v68, v70, v71
	v_cvt_pk_bf16_f32 v93, v96, v97
	v_cvt_pk_bf16_f32 v69, v72, v73
	ds_read_b128 v[70:73], v212 offset:14336
	v_pk_max_i16 v90, v90, 0
	v_pk_max_i16 v91, v91, 0
	v_pk_max_i16 v92, v92, 0
	v_pk_max_i16 v93, v93, 0
	v_pk_max_i16 v66, v66, 0
	v_pk_max_i16 v67, v67, 0
	v_pk_max_i16 v68, v68, 0
	v_pk_max_i16 v69, v69, 0
	v_cvt_pk_bf16_f32 v96, v102, v103
	s_waitcnt lgkmcnt(2)
	v_mfma_f32_32x32x16_bf16 v[2:17], v[110:113], v[90:93], v[2:17]
	v_cvt_pk_bf16_f32 v97, v104, v105
	v_cvt_pk_bf16_f32 v74, v74, v75
	v_cvt_pk_bf16_f32 v75, v76, v77
	v_cvt_pk_bf16_f32 v76, v78, v79
	v_cvt_pk_bf16_f32 v77, v80, v81
	v_pk_max_i16 v94, v94, 0
	v_pk_max_i16 v95, v95, 0
	v_pk_max_i16 v96, v96, 0
	v_pk_max_i16 v97, v97, 0
	v_pk_max_i16 v74, v74, 0
	v_pk_max_i16 v75, v75, 0
	v_pk_max_i16 v76, v76, 0
	v_pk_max_i16 v77, v77, 0
	v_mfma_f32_32x32x16_bf16 v[18:33], v[110:113], v[66:69], v[18:33]
	s_waitcnt lgkmcnt(1)
	v_mfma_f32_32x32x16_bf16 v[34:49], v[98:101], v[66:69], v[34:49]
	ds_read_b128 v[66:69], v212 offset:22528
	v_mfma_f32_32x32x16_bf16 v[50:65], v[98:101], v[90:93], v[50:65]
	s_waitcnt lgkmcnt(1)
	v_mfma_f32_32x32x16_bf16 v[2:17], v[70:73], v[94:97], v[2:17]
	v_mfma_f32_32x32x16_bf16 v[18:33], v[70:73], v[74:77], v[18:33]
	ds_read_b128 v[78:81], v212 offset:3072
	s_waitcnt lgkmcnt(1)
	v_mfma_f32_32x32x16_bf16 v[50:65], v[66:69], v[94:97], v[50:65]
	ds_read_b128 v[90:93], v174 offset:33056
	ds_read_b128 v[94:97], v174 offset:33088
	ds_read_b128 v[98:101], v174 offset:33120
	ds_read_b128 v[70:73], v174 offset:33152
	v_mfma_f32_32x32x16_bf16 v[34:49], v[66:69], v[74:77], v[34:49]
	ds_read_b128 v[66:69], v212 offset:4096
	ds_read_b128 v[74:77], v212 offset:5120
	s_waitcnt lgkmcnt(3)
	v_mfma_f32_32x32x16_bf16 v[102:117], v[78:81], v[126:129], v[86:101]
	v_mfma_f32_32x32x16_bf16 v[86:101], v[78:81], v[134:137], v[86:101]
	s_waitcnt lgkmcnt(1)
	v_mfma_f32_32x32x16_bf16 v[86:101], v[66:69], v[146:149], v[86:101]
	v_mfma_f32_32x32x16_bf16 v[102:117], v[66:69], v[122:125], v[102:117]
	ds_read_b128 v[66:69], v212 offset:6144
	s_waitcnt lgkmcnt(1)
	v_mfma_f32_32x32x16_bf16 v[86:101], v[74:77], v[142:145], v[86:101]
	v_mfma_f32_32x32x16_bf16 v[102:117], v[74:77], v[130:133], v[102:117]
	ds_read_b128 v[74:77], v212 offset:15360
	s_waitcnt lgkmcnt(1)
	v_mfma_f32_32x32x16_bf16 v[86:101], v[66:69], v[138:141], v[86:101]
	v_mfma_f32_32x32x16_bf16 v[102:117], v[66:69], v[118:121], v[102:117]
	s_nop 10
	v_cvt_pk_bf16_f32 v78, v86, v87
	v_cvt_pk_bf16_f32 v80, v90, v91
	v_cvt_pk_bf16_f32 v79, v88, v89
	v_cvt_pk_bf16_f32 v81, v92, v93
	ds_read_b128 v[86:89], v212 offset:16384
	ds_read_b128 v[90:93], v212 offset:23552
	v_cvt_pk_bf16_f32 v66, v102, v103
	v_cvt_pk_bf16_f32 v67, v104, v105
	v_cvt_pk_bf16_f32 v68, v106, v107
	v_cvt_pk_bf16_f32 v69, v108, v109
	v_pk_max_i16 v66, v66, 0
	v_pk_max_i16 v67, v67, 0
	v_pk_max_i16 v68, v68, 0
	v_pk_max_i16 v69, v69, 0
	v_pk_max_i16 v78, v78, 0
	v_pk_max_i16 v79, v79, 0
	v_pk_max_i16 v80, v80, 0
	v_pk_max_i16 v81, v81, 0
	v_cvt_pk_bf16_f32 v94, v94, v95
	s_waitcnt lgkmcnt(2)
	v_mfma_f32_32x32x16_bf16 v[18:33], v[74:77], v[78:81], v[18:33]
	v_cvt_pk_bf16_f32 v95, v96, v97
	v_cvt_pk_bf16_f32 v96, v98, v99
	v_cvt_pk_bf16_f32 v97, v100, v101
	v_pk_max_i16 v94, v94, 0
	v_pk_max_i16 v95, v95, 0
	v_pk_max_i16 v96, v96, 0
	v_pk_max_i16 v97, v97, 0
	v_mfma_f32_32x32x16_bf16 v[2:17], v[74:77], v[66:69], v[2:17]
	v_cvt_pk_bf16_f32 v74, v110, v111
	v_cvt_pk_bf16_f32 v75, v112, v113
	v_cvt_pk_bf16_f32 v76, v114, v115
	v_cvt_pk_bf16_f32 v77, v116, v117
	v_pk_max_i16 v74, v74, 0
	v_pk_max_i16 v75, v75, 0
	v_pk_max_i16 v76, v76, 0
	v_pk_max_i16 v77, v77, 0
	s_waitcnt lgkmcnt(0)
	v_mfma_f32_32x32x16_bf16 v[50:65], v[90:93], v[66:69], v[50:65]
	ds_read_b128 v[66:69], v212 offset:24576
	v_mfma_f32_32x32x16_bf16 v[34:49], v[90:93], v[78:81], v[34:49]
	ds_read_b128 v[102:105], v212 offset:7168
	v_mfma_f32_32x32x16_bf16 v[2:17], v[86:89], v[74:77], v[2:17]
	s_waitcnt lgkmcnt(1)
	v_mfma_f32_32x32x16_bf16 v[50:65], v[66:69], v[74:77], v[50:65]
	ds_read_b128 v[74:77], v174 offset:33184
	ds_read_b128 v[78:81], v174 offset:33216
	v_mfma_f32_32x32x16_bf16 v[34:49], v[66:69], v[94:97], v[34:49]
	ds_read_b128 v[66:69], v212 offset:8192
	v_mfma_f32_32x32x16_bf16 v[18:33], v[86:89], v[94:97], v[18:33]
	s_waitcnt lgkmcnt(1)
	v_mfma_f32_32x32x16_bf16 v[86:101], v[102:105], v[126:129], v[70:85]
	v_mfma_f32_32x32x16_bf16 v[70:85], v[102:105], v[134:137], v[70:85]
	ds_read_b128 v[102:105], v212 offset:9216
	v_lshlrev_b32_e32 v135, 2, v1
	v_add_u32_e32 v134, v172, v174
	s_waitcnt lgkmcnt(1)
	v_mfma_f32_32x32x16_bf16 v[86:101], v[66:69], v[122:125], v[86:101]
	v_mfma_f32_32x32x16_bf16 v[70:85], v[66:69], v[146:149], v[70:85]
	ds_read_b128 v[66:69], v212 offset:10240
	s_waitcnt lgkmcnt(1)
	v_mfma_f32_32x32x16_bf16 v[86:101], v[102:105], v[130:133], v[86:101]
	v_mfma_f32_32x32x16_bf16 v[70:85], v[102:105], v[142:145], v[70:85]
	ds_read_b128 v[102:105], v212 offset:17408
	s_waitcnt lgkmcnt(1)
	v_mfma_f32_32x32x16_bf16 v[86:101], v[66:69], v[118:121], v[86:101]
	v_mfma_f32_32x32x16_bf16 v[70:85], v[66:69], v[138:141], v[70:85]
	s_nop 10
	v_cvt_pk_bf16_f32 v68, v90, v91
	v_cvt_pk_bf16_f32 v69, v92, v93
	ds_read_b128 v[90:93], v212 offset:25600
	v_cvt_pk_bf16_f32 v66, v86, v87
	v_cvt_pk_bf16_f32 v67, v88, v89
	v_pk_max_i16 v66, v66, 0
	v_pk_max_i16 v67, v67, 0
	v_pk_max_i16 v68, v68, 0
	v_pk_max_i16 v69, v69, 0
	v_cvt_pk_bf16_f32 v70, v70, v71
	v_cvt_pk_bf16_f32 v71, v72, v73
	s_waitcnt lgkmcnt(1)
	v_mfma_f32_32x32x16_bf16 v[2:17], v[102:105], v[66:69], v[2:17]
	v_cvt_pk_bf16_f32 v72, v74, v75
	v_cvt_pk_bf16_f32 v73, v76, v77
	ds_read_b128 v[74:77], v212 offset:18432
	v_cvt_pk_bf16_f32 v86, v94, v95
	v_cvt_pk_bf16_f32 v87, v96, v97
	v_cvt_pk_bf16_f32 v88, v98, v99
	s_waitcnt lgkmcnt(1)
	v_mfma_f32_32x32x16_bf16 v[50:65], v[90:93], v[66:69], v[50:65]
	ds_read_b128 v[66:69], v212 offset:26624
	v_cvt_pk_bf16_f32 v89, v100, v101
	v_pk_max_i16 v86, v86, 0
	v_pk_max_i16 v87, v87, 0
	v_pk_max_i16 v88, v88, 0
	v_pk_max_i16 v89, v89, 0
	v_pk_max_i16 v70, v70, 0
	v_pk_max_i16 v71, v71, 0
	v_pk_max_i16 v72, v72, 0
	v_pk_max_i16 v73, v73, 0
	v_cvt_pk_bf16_f32 v78, v78, v79
	v_cvt_pk_bf16_f32 v79, v80, v81
	s_waitcnt lgkmcnt(1)
	v_mfma_f32_32x32x16_bf16 v[2:17], v[74:77], v[86:89], v[2:17]
	v_cvt_pk_bf16_f32 v80, v82, v83
	v_cvt_pk_bf16_f32 v81, v84, v85
	v_pk_max_i16 v78, v78, 0
	v_pk_max_i16 v79, v79, 0
	v_pk_max_i16 v80, v80, 0
	v_pk_max_i16 v81, v81, 0
	s_waitcnt lgkmcnt(0)
	v_mfma_f32_32x32x16_bf16 v[50:65], v[66:69], v[86:89], v[50:65]
	v_mfma_f32_32x32x16_bf16 v[34:49], v[90:93], v[70:73], v[34:49]
	s_nop 10
	v_add_f32_e32 v130, v10, v58
	v_add_f32_e32 v131, v11, v59
	v_add_f32_e32 v132, v12, v60
	v_add_f32_e32 v133, v13, v61
	v_add_f32_e32 v138, v4, v52
	v_add_f32_e32 v139, v5, v53
	v_pk_add_f32 v[140:141], v[16:17], v[64:65]
	v_pk_add_f32 v[142:143], v[8:9], v[56:57]
	v_pk_add_f32 v[144:145], v[14:15], v[62:63]
	v_pk_add_f32 v[146:147], v[6:7], v[54:55]
	v_mfma_f32_32x32x16_bf16 v[18:33], v[102:105], v[70:73], v[18:33]
	ds_read2st64_b32 v[70:71], v135 offset0:133 offset1:134
	v_add_f32_e32 v148, v2, v50
	v_add_f32_e32 v149, v3, v51
	v_add_f32_e32 v144, v146, v144
	v_add_f32_e32 v145, v147, v145
	v_pk_add_f32 v[140:141], v[142:143], v[140:141]
	v_pk_add_f32 v[132:133], v[138:139], v[132:133]
	v_pk_add_f32 v[130:131], v[148:149], v[130:131]
	v_pk_add_f32 v[132:133], v[132:133], v[140:141]
	v_pk_add_f32 v[130:131], v[130:131], v[144:145]
	v_mfma_f32_32x32x16_bf16 v[34:49], v[66:69], v[78:81], v[34:49]
	v_pk_mov_b32 v[138:139], v[130:131], v[132:133] op_sel:[1,0]
	v_mov_b32_e32 v131, v133
	s_waitcnt vmcnt(0) lgkmcnt(0)
	v_mul_f32_e32 v66, v175, v70
	v_pk_add_f32 v[130:131], v[138:139], v[130:131]
	ds_write_b32 v173, v66 offset:512
	v_mul_f32_e32 v66, v175, v71
	v_pk_add_f32 v[130:131], v[130:131], v[130:131] op_sel:[0,1] op_sel_hi:[1,0]
	s_waitcnt lgkmcnt(0)
	ds_read_b128 v[102:105], v174 offset:34560
	ds_read_b128 v[98:101], v174 offset:34592
	ds_read_b128 v[110:113], v174 offset:34624
	ds_read_b128 v[106:109], v174 offset:34656
	ds_read_b128 v[114:117], v174 offset:34688
	ds_read_b128 v[122:125], v174 offset:34720
	ds_read_b128 v[118:121], v174 offset:34752
	ds_read_b128 v[126:129], v174 offset:34784
	v_mov_b32_dpp v66, v66 quad_perm:[1,0,3,2] row_mask:0xf bank_mask:0xf bound_ctrl:1
	v_mov_b32_e32 v131, v130
	v_fmac_f32_e32 v66, v175, v71
	s_nop 0
	v_permlane32_swap_b32_e32 v130, v131
	v_add_f32_dpp v66, v66, v66 quad_perm:[2,3,0,1] row_mask:0xf bank_mask:0xf bound_ctrl:1
	v_add_f32_e32 v130, v130, v131
	v_fmamk_f32 v65, v130, 0xbc800000, v65
	v_add_f32_dpp v66, v66, v66 row_half_mirror row_mask:0xf bank_mask:0xf bound_ctrl:1
	v_fmamk_f32 v64, v130, 0xbc800000, v64
	v_fmamk_f32 v63, v130, 0xbc800000, v63
	v_fmamk_f32 v62, v130, 0xbc800000, v62
	v_fmamk_f32 v61, v130, 0xbc800000, v61
	v_fmamk_f32 v60, v130, 0xbc800000, v60
	v_fmamk_f32 v59, v130, 0xbc800000, v59
	v_fmamk_f32 v58, v130, 0xbc800000, v58
	v_fmamk_f32 v57, v130, 0xbc800000, v57
	v_fmamk_f32 v56, v130, 0xbc800000, v56
	v_fmamk_f32 v55, v130, 0xbc800000, v55
	v_fmamk_f32 v54, v130, 0xbc800000, v54
	v_fmamk_f32 v53, v130, 0xbc800000, v53
	v_fmamk_f32 v52, v130, 0xbc800000, v52
	v_fmamk_f32 v51, v130, 0xbc800000, v51
	v_fmac_f32_e32 v50, 0xbc800000, v130
	v_add_f32_dpp v66, v66, v66 row_ror:8 row_mask:0xf bank_mask:0xf bound_ctrl:1
	v_fmamk_f32 v17, v130, 0xbc800000, v17
	v_fmamk_f32 v16, v130, 0xbc800000, v16
	v_fmamk_f32 v15, v130, 0xbc800000, v15
	v_fmamk_f32 v14, v130, 0xbc800000, v14
	v_fmamk_f32 v13, v130, 0xbc800000, v13
	v_fmamk_f32 v12, v130, 0xbc800000, v12
	v_fmamk_f32 v11, v130, 0xbc800000, v11
	v_fmamk_f32 v10, v130, 0xbc800000, v10
	v_fmamk_f32 v9, v130, 0xbc800000, v9
	v_fmamk_f32 v8, v130, 0xbc800000, v8
	v_fmamk_f32 v7, v130, 0xbc800000, v7
	v_fmamk_f32 v6, v130, 0xbc800000, v6
	v_fmamk_f32 v5, v130, 0xbc800000, v5
	v_fmamk_f32 v4, v130, 0xbc800000, v4
	v_fmamk_f32 v3, v130, 0xbc800000, v3
	v_fmac_f32_e32 v2, 0xbc800000, v130
	v_pk_mul_f32 v[130:131], v[54:55], v[54:55]
	v_pk_mul_f32 v[132:133], v[62:63], v[62:63]
	v_pk_mul_f32 v[138:139], v[50:51], v[50:51]
	v_pk_mul_f32 v[140:141], v[58:59], v[58:59]
	v_pk_mul_f32 v[142:143], v[56:57], v[56:57]
	v_pk_mul_f32 v[144:145], v[64:65], v[64:65]
	v_pk_mul_f32 v[146:147], v[52:53], v[52:53]
	v_pk_mul_f32 v[148:149], v[60:61], v[60:61]
	v_mov_b32_e32 v67, v66
	v_pk_fma_f32 v[148:149], v[12:13], v[12:13], v[148:149]
	v_pk_fma_f32 v[146:147], v[4:5], v[4:5], v[146:147]
	v_pk_fma_f32 v[144:145], v[16:17], v[16:17], v[144:145]
	v_pk_fma_f32 v[142:143], v[8:9], v[8:9], v[142:143]
	v_pk_fma_f32 v[140:141], v[10:11], v[10:11], v[140:141]
	v_pk_fma_f32 v[138:139], v[2:3], v[2:3], v[138:139]
	v_pk_fma_f32 v[132:133], v[14:15], v[14:15], v[132:133]
	v_pk_fma_f32 v[130:131], v[6:7], v[6:7], v[130:131]
	v_permlane16_swap_b32_e32 v66, v67
	v_pk_add_f32 v[130:131], v[130:131], v[132:133]
	v_pk_add_f32 v[132:133], v[138:139], v[140:141]
	v_pk_add_f32 v[138:139], v[142:143], v[144:145]
	v_pk_add_f32 v[140:141], v[146:147], v[148:149]
	v_mfma_f32_32x32x16_bf16 v[18:33], v[74:77], v[78:81], v[18:33]
	v_add_f32_e32 v136, v66, v67
	ds_read_b128 v[70:73], v134 offset:512
	ds_read_b128 v[66:69], v134 offset:544
	ds_read_b128 v[78:81], v134 offset:576
	ds_read_b128 v[74:77], v134 offset:608
	ds_read_b128 v[82:85], v134 offset:640
	ds_read_b128 v[90:93], v134 offset:672
	ds_read_b128 v[86:89], v134 offset:704
	ds_read_b128 v[94:97], v134 offset:736
	v_pk_add_f32 v[138:139], v[140:141], v[138:139]
	v_pk_add_f32 v[130:131], v[132:133], v[130:131]
	s_waitcnt lgkmcnt(8)
	v_pk_mul_f32 v[140:141], v[126:127], v[62:63]
	v_pk_mov_b32 v[132:133], v[130:131], v[138:139] op_sel:[1,0]
	v_mov_b32_e32 v131, v139
	v_pk_mul_f32 v[138:139], v[122:123], v[54:55]
	v_pk_mul_f32 v[142:143], v[114:115], v[50:51]
	v_pk_mul_f32 v[144:145], v[118:119], v[58:59]
	v_pk_mul_f32 v[146:147], v[124:125], v[56:57]
	v_pk_mul_f32 v[148:149], v[128:129], v[64:65]
	v_pk_mul_f32 v[154:155], v[116:117], v[52:53]
	v_pk_mul_f32 v[156:157], v[120:121], v[60:61]
	v_pk_fma_f32 v[154:155], v[104:105], v[4:5], v[154:155]
	v_pk_fma_f32 v[156:157], v[112:113], v[12:13], v[156:157]
	v_pk_fma_f32 v[148:149], v[108:109], v[16:17], v[148:149]
	v_pk_fma_f32 v[146:147], v[100:101], v[8:9], v[146:147]
	v_pk_fma_f32 v[144:145], v[110:111], v[10:11], v[144:145]
	v_pk_fma_f32 v[142:143], v[102:103], v[2:3], v[142:143]
	v_pk_fma_f32 v[140:141], v[106:107], v[14:15], v[140:141]
	v_pk_fma_f32 v[138:139], v[98:99], v[6:7], v[138:139]
	v_pk_add_f32 v[130:131], v[132:133], v[130:131]
	v_pk_add_f32 v[138:139], v[138:139], v[140:141]
	v_pk_add_f32 v[140:141], v[142:143], v[144:145]
	v_pk_add_f32 v[142:143], v[146:147], v[148:149]
	v_pk_add_f32 v[144:145], v[154:155], v[156:157]
	v_pk_add_f32 v[132:133], v[130:131], v[130:131] op_sel:[0,1] op_sel_hi:[1,0]
	v_pk_add_f32 v[142:143], v[144:145], v[142:143]
	v_pk_add_f32 v[138:139], v[140:141], v[138:139]
	v_add_f32_e32 v133, v142, v143
	v_add_f32_e32 v130, v138, v139
	s_waitcnt lgkmcnt(2)
	v_pk_mul_f32 v[138:139], v[90:91], v[54:55]
	s_waitcnt lgkmcnt(0)
	v_pk_mul_f32 v[140:141], v[94:95], v[62:63]
	v_pk_mul_f32 v[142:143], v[82:83], v[50:51]
	v_pk_mul_f32 v[144:145], v[86:87], v[58:59]
	v_pk_mul_f32 v[146:147], v[92:93], v[56:57]
	v_pk_mul_f32 v[148:149], v[96:97], v[64:65]
	v_pk_mul_f32 v[154:155], v[84:85], v[52:53]
	v_pk_mul_f32 v[156:157], v[88:89], v[60:61]
	v_add_f32_e32 v130, v130, v133
	v_pk_fma_f32 v[156:157], v[80:81], v[12:13], v[156:157]
	v_pk_fma_f32 v[154:155], v[72:73], v[4:5], v[154:155]
	v_pk_fma_f32 v[148:149], v[76:77], v[16:17], v[148:149]
	v_pk_fma_f32 v[146:147], v[68:69], v[8:9], v[146:147]
	v_pk_fma_f32 v[144:145], v[78:79], v[10:11], v[144:145]
	v_pk_fma_f32 v[142:143], v[70:71], v[2:3], v[142:143]
	v_pk_fma_f32 v[140:141], v[74:75], v[14:15], v[140:141]
	v_pk_fma_f32 v[138:139], v[66:67], v[6:7], v[138:139]
	v_mov_b32_e32 v133, v130
	v_pk_add_f32 v[138:139], v[138:139], v[140:141]
	v_pk_add_f32 v[140:141], v[142:143], v[144:145]
	v_pk_add_f32 v[142:143], v[146:147], v[148:149]
	v_pk_add_f32 v[144:145], v[154:155], v[156:157]
	v_permlane32_swap_b32_e32 v130, v133
	v_pk_add_f32 v[142:143], v[144:145], v[142:143]
	v_add_f32_e32 v160, v130, v133
	v_pk_add_f32 v[138:139], v[140:141], v[138:139]
	v_add_f32_e32 v133, v142, v143
	v_pk_add_f32 v[140:141], v[26:27], v[42:43]
	v_pk_add_f32 v[142:143], v[28:29], v[44:45]
	v_pk_add_f32 v[144:145], v[20:21], v[36:37]
	v_pk_add_f32 v[146:147], v[32:33], v[48:49]
	v_pk_add_f32 v[148:149], v[24:25], v[40:41]
	v_pk_add_f32 v[154:155], v[30:31], v[46:47]
	v_pk_add_f32 v[156:157], v[22:23], v[38:39]
	v_pk_add_f32 v[158:159], v[18:19], v[34:35]
	v_pk_add_f32 v[154:155], v[156:157], v[154:155]
	v_pk_add_f32 v[146:147], v[148:149], v[146:147]
	v_pk_add_f32 v[142:143], v[144:145], v[142:143]
	v_pk_add_f32 v[140:141], v[158:159], v[140:141]
	v_pk_add_f32 v[142:143], v[142:143], v[146:147]
	v_pk_add_f32 v[140:141], v[140:141], v[154:155]
	v_add_f32_e32 v130, v138, v139
	v_pk_mov_b32 v[144:145], v[140:141], v[142:143] op_sel:[1,0]
	v_mov_b32_e32 v141, v143
	v_pk_add_f32 v[140:141], v[144:145], v[140:141]
	v_add_f32_e32 v133, v130, v133
	v_pk_add_f32 v[140:141], v[140:141], v[140:141] op_sel:[0,1] op_sel_hi:[1,0]
	v_mov_b32_e32 v131, v132
	v_mov_b32_e32 v130, v140
	s_nop 1
	v_permlane32_swap_b32_e32 v140, v130
	v_add_f32_e32 v130, v140, v130
	v_fmamk_f32 v49, v130, 0xbc800000, v49
	v_fmamk_f32 v48, v130, 0xbc800000, v48
	v_fmamk_f32 v47, v130, 0xbc800000, v47
	v_fmamk_f32 v46, v130, 0xbc800000, v46
	v_fmamk_f32 v45, v130, 0xbc800000, v45
	v_fmamk_f32 v44, v130, 0xbc800000, v44
	v_fmamk_f32 v43, v130, 0xbc800000, v43
	v_fmamk_f32 v42, v130, 0xbc800000, v42
	v_fmamk_f32 v41, v130, 0xbc800000, v41
	v_fmamk_f32 v40, v130, 0xbc800000, v40
	v_fmamk_f32 v39, v130, 0xbc800000, v39
	v_fmamk_f32 v38, v130, 0xbc800000, v38
	v_fmamk_f32 v37, v130, 0xbc800000, v37
	v_fmamk_f32 v36, v130, 0xbc800000, v36
	v_fmamk_f32 v35, v130, 0xbc800000, v35
	v_fmac_f32_e32 v34, 0xbc800000, v130
	v_fmamk_f32 v33, v130, 0xbc800000, v33
	v_fmamk_f32 v32, v130, 0xbc800000, v32
	v_fmamk_f32 v31, v130, 0xbc800000, v31
	v_fmamk_f32 v30, v130, 0xbc800000, v30
	v_fmamk_f32 v29, v130, 0xbc800000, v29
	v_fmamk_f32 v28, v130, 0xbc800000, v28
	v_fmamk_f32 v27, v130, 0xbc800000, v27
	v_fmamk_f32 v26, v130, 0xbc800000, v26
	v_fmamk_f32 v25, v130, 0xbc800000, v25
	v_fmamk_f32 v24, v130, 0xbc800000, v24
	v_fmamk_f32 v23, v130, 0xbc800000, v23
	v_fmamk_f32 v22, v130, 0xbc800000, v22
	v_fmamk_f32 v21, v130, 0xbc800000, v21
	v_fmamk_f32 v20, v130, 0xbc800000, v20
	v_fmamk_f32 v19, v130, 0xbc800000, v19
	v_fmac_f32_e32 v18, 0xbc800000, v130
	v_pk_mul_f32 v[140:141], v[38:39], v[38:39]
	v_pk_mul_f32 v[142:143], v[46:47], v[46:47]
	v_pk_mul_f32 v[144:145], v[34:35], v[34:35]
	v_pk_mul_f32 v[146:147], v[42:43], v[42:43]
	v_pk_mul_f32 v[148:149], v[40:41], v[40:41]
	v_pk_mul_f32 v[154:155], v[48:49], v[48:49]
	v_pk_mul_f32 v[156:157], v[36:37], v[36:37]
	v_pk_mul_f32 v[158:159], v[44:45], v[44:45]
	v_pk_fma_f32 v[156:157], v[20:21], v[20:21], v[156:157]
	v_pk_fma_f32 v[158:159], v[28:29], v[28:29], v[158:159]
	v_pk_fma_f32 v[154:155], v[32:33], v[32:33], v[154:155]
	v_pk_fma_f32 v[148:149], v[24:25], v[24:25], v[148:149]
	v_pk_fma_f32 v[146:147], v[26:27], v[26:27], v[146:147]
	v_pk_fma_f32 v[144:145], v[18:19], v[18:19], v[144:145]
	v_pk_fma_f32 v[142:143], v[30:31], v[30:31], v[142:143]
	v_pk_fma_f32 v[140:141], v[22:23], v[22:23], v[140:141]
	v_permlane32_swap_b32_e32 v132, v131
	v_pk_add_f32 v[140:141], v[140:141], v[142:143]
	v_pk_add_f32 v[142:143], v[144:145], v[146:147]
	v_pk_add_f32 v[144:145], v[148:149], v[154:155]
	v_pk_add_f32 v[146:147], v[156:157], v[158:159]
	v_pk_add_f32 v[140:141], v[142:143], v[140:141]
	v_pk_add_f32 v[144:145], v[146:147], v[144:145]
	v_pk_mul_f32 v[122:123], v[122:123], v[38:39]
	v_pk_mov_b32 v[142:143], v[140:141], v[144:145] op_sel:[1,0]
	v_mov_b32_e32 v141, v145
	v_pk_add_f32 v[140:141], v[142:143], v[140:141]
	v_pk_mul_f32 v[126:127], v[126:127], v[46:47]
	v_pk_add_f32 v[140:141], v[140:141], v[140:141] op_sel:[0,1] op_sel_hi:[1,0]
	v_pk_mul_f32 v[114:115], v[114:115], v[34:35]
	v_mov_b32_e32 v130, v140
	s_nop 1
	v_permlane32_swap_b32_e32 v140, v130
	v_mov_b32_e32 v141, v132
	v_pk_add_f32 v[130:131], v[140:141], v[130:131]
	v_pk_mul_f32 v[118:119], v[118:119], v[42:43]
	v_pk_fma_f32 v[130:131], v[130:131], s[0:1], v[152:153] op_sel_hi:[1,0,0]
	v_pk_mul_f32 v[124:125], v[124:125], v[40:41]
	v_mul_f32_e32 v132, 0x4b800000, v131
	v_cmp_gt_f32_e32 vcc, s1, v131
	v_pk_mul_f32 v[128:129], v[128:129], v[48:49]
	v_pk_mul_f32 v[116:117], v[116:117], v[36:37]
	v_pk_mul_f32 v[120:121], v[120:121], v[44:45]
	v_cndmask_b32_e32 v131, v131, v132, vcc
	v_mul_f32_e32 v132, 0x4b800000, v130
	v_cmp_gt_f32_e64 s[0:1], s1, v130
	v_pk_fma_f32 v[112:113], v[112:113], v[28:29], v[120:121]
	v_pk_fma_f32 v[104:105], v[104:105], v[20:21], v[116:117]
	v_pk_fma_f32 v[108:109], v[108:109], v[32:33], v[128:129]
	v_pk_fma_f32 v[100:101], v[100:101], v[24:25], v[124:125]
	v_pk_fma_f32 v[110:111], v[110:111], v[26:27], v[118:119]
	v_pk_fma_f32 v[102:103], v[102:103], v[18:19], v[114:115]
	v_pk_fma_f32 v[106:107], v[106:107], v[30:31], v[126:127]
	v_pk_fma_f32 v[98:99], v[98:99], v[22:23], v[122:123]
	v_rsq_f32_e32 v131, v131
	v_cndmask_b32_e64 v130, v130, v132, s[0:1]
	v_pk_add_f32 v[98:99], v[98:99], v[106:107]
	v_pk_add_f32 v[102:103], v[102:103], v[110:111]
	v_pk_add_f32 v[100:101], v[100:101], v[108:109]
	v_pk_add_f32 v[104:105], v[104:105], v[112:113]
	v_rsq_f32_e32 v132, v130
	v_pk_add_f32 v[100:101], v[104:105], v[100:101]
	v_pk_add_f32 v[98:99], v[102:103], v[98:99]
	v_mul_f32_e32 v130, 0x45800000, v131
	v_add_f32_e32 v98, v98, v99
	v_add_f32_e32 v99, v100, v101
	v_add_f32_e32 v98, v98, v99
	v_mov_b32_e32 v99, v98
	v_pk_mul_f32 v[90:91], v[90:91], v[38:39]
	v_pk_mul_f32 v[94:95], v[94:95], v[46:47]
	v_pk_mul_f32 v[82:83], v[82:83], v[34:35]
	v_pk_mul_f32 v[86:87], v[86:87], v[42:43]
	v_cndmask_b32_e32 v130, v131, v130, vcc
	v_mul_f32_e32 v131, 0x45800000, v132
	v_permlane32_swap_b32_e32 v98, v99
	v_pk_fma_f32 v[78:79], v[78:79], v[26:27], v[86:87]
	v_pk_fma_f32 v[70:71], v[70:71], v[18:19], v[82:83]
	v_pk_fma_f32 v[74:75], v[74:75], v[30:31], v[94:95]
	v_pk_fma_f32 v[66:67], v[66:67], v[22:23], v[90:91]
	v_cndmask_b32_e64 v131, v132, v131, s[0:1]
	v_add_f32_e32 v98, v98, v99
	v_pk_add_f32 v[66:67], v[66:67], v[74:75]
	v_pk_add_f32 v[70:71], v[70:71], v[78:79]
	v_mul_f32_e32 v139, v160, v130
	v_mul_f32_e32 v98, v98, v131
	v_pk_add_f32 v[66:67], v[70:71], v[66:67]
	v_cmp_gt_u32_e32 vcc, 32, v1
	v_add_f32_e32 v66, v66, v67
	v_pk_mul_f32 v[92:93], v[92:93], v[40:41]
	v_cndmask_b32_e32 v67, v98, v139, vcc
	v_add_f32_e32 v67, s12, v67
	v_pk_mul_f32 v[96:97], v[96:97], v[48:49]
	v_pk_mul_f32 v[84:85], v[84:85], v[36:37]
	v_pk_mul_f32 v[88:89], v[88:89], v[44:45]
	v_mul_f32_e32 v67, 0xbfb8aa3b, v67
	v_pk_fma_f32 v[80:81], v[80:81], v[28:29], v[88:89]
	v_pk_fma_f32 v[72:73], v[72:73], v[20:21], v[84:85]
	v_pk_fma_f32 v[76:77], v[76:77], v[32:33], v[96:97]
	v_pk_fma_f32 v[68:69], v[68:69], v[24:25], v[92:93]
	v_exp_f32_e32 v70, v67
	v_pk_add_f32 v[68:69], v[68:69], v[76:77]
	v_pk_add_f32 v[72:73], v[72:73], v[80:81]
	v_cmp_lt_i32_e64 s[0:1], 0, v151
	v_pk_add_f32 v[68:69], v[72:73], v[68:69]
	v_mov_b32_e32 v137, v136
	v_add_f32_e32 v67, v68, v69
	v_add_f32_e32 v67, v66, v67
	v_add_f32_e32 v66, 1.0, v70
	v_rcp_f32_e32 v66, v66
	v_mov_b32_e32 v69, 0xff800000
	v_mov_b32_e32 v138, v133
	v_mov_b32_e32 v68, v67
	v_cndmask_b32_e64 v70, v69, v66, s[0:1]
	v_mbcnt_lo_u32_b32 v66, -1, 0
	v_mbcnt_hi_u32_b32 v66, -1, v66
	v_permlane32_swap_b32_e32 v136, v137
	v_permlane32_swap_b32_e32 v133, v138
	v_permlane32_swap_b32_e32 v67, v68
	v_and_b32_e32 v86, 64, v66
	s_mov_b32 s14, 8
	s_mov_b32 s13, 0
	v_mov_b32_e32 v66, 0
	s_waitcnt lgkmcnt(0)
